# NA attention: half tiles outside a wave's column half handle only the 4 score slots that can be in-window (trimmed lookup/mask/softmax copy)
# baseline (speedup 1.0000x reference)
.Lna_minor_1:
	ds_read_b32 v66, v237 offset:128
	ds_read_b32 v67, v237 offset:132
	ds_read_b32 v68, v237 offset:136
	ds_read_b32 v69, v237 offset:140
	s_waitcnt lgkmcnt(0)
	v_cmp_ge_i32_e32 vcc, v219, v245
	v_cmp_lt_i32_e64 s[12:13], v219, v246
	s_and_b64 vcc, vcc, s[12:13]
	v_fmac_f32_e32 v66, 0x3e0293ee, v82
	v_cndmask_b32_e32 v66, v222, v66, vcc
	v_cmp_ge_i32_e32 vcc, v220, v245
	v_cmp_lt_i32_e64 s[12:13], v220, v246
	s_and_b64 vcc, vcc, s[12:13]
	v_fmac_f32_e32 v67, 0x3e0293ee, v83
	v_cndmask_b32_e32 v67, v222, v67, vcc
	v_cmp_ge_i32_e32 vcc, v221, v245
	v_cmp_lt_i32_e64 s[12:13], v221, v246
	s_and_b64 vcc, vcc, s[12:13]
	v_fmac_f32_e32 v68, 0x3e0293ee, v84
	v_cndmask_b32_e32 v68, v222, v68, vcc
	v_cmp_ge_i32_e32 vcc, v223, v245
	v_cmp_lt_i32_e64 s[12:13], v223, v246
	s_and_b64 vcc, vcc, s[12:13]
	v_fmac_f32_e32 v69, 0x3e0293ee, v85
	v_cndmask_b32_e32 v69, v222, v69, vcc
	v_max_f32_e32 v82, v66, v67
	v_max3_f32 v82, v82, v68, v69
	v_mov_b32_e32 v83, v82
	s_nop 1
	v_permlane32_swap_b32_e32 v82, v83
	v_max_f32_e32 v82, v82, v83
	v_sub_f32_e32 v83, v82, v244
	v_cmp_ge_f32_e32 vcc, s63, v83
	s_cmp_eq_u64 vcc, exec
	v_max_f32_e32 v82, v244, v82
	s_cselect_b64 vcc, -1, 0
	v_sub_f32_e32 v83, v244, v82
	v_cndmask_b32_e32 v244, v82, v244, vcc
	v_exp_f32_e32 v83, v83
	v_sub_f32_e32 v66, v66, v244
	v_exp_f32_e32 v66, v66
	v_sub_f32_e32 v67, v67, v244
	v_exp_f32_e32 v67, v67
	v_sub_f32_e32 v68, v68, v244
	v_exp_f32_e32 v68, v68
	v_sub_f32_e32 v69, v69, v244
	v_exp_f32_e32 v69, v69
	v_add_f32_e32 v82, v66, v67
	v_add_f32_e32 v82, v68, v82
	v_add_f32_e32 v75, v69, v82
	v_cndmask_b32_e64 v74, v83, 1.0, vcc
	v_mov_b32_e32 v76, v75
	v_cvt_pk_bf16_f32 v66, v66, v67
	v_cvt_pk_bf16_f32 v67, v68, v69
	v_mov_b32_e32 v68, 0
	v_mov_b32_e32 v69, 0
	v_mov_b32_e32 v70, 0
	v_mov_b32_e32 v71, 0
	v_mov_b32_e32 v72, 0
	v_mov_b32_e32 v73, 0
	s_branch .Lna_join_1
.Lna_minor_0:
	ds_read_b32 v78, v237 offset:96
	ds_read_b32 v79, v237 offset:100
	ds_read_b32 v80, v237 offset:104
	ds_read_b32 v81, v237 offset:108
	s_waitcnt lgkmcnt(0)
	v_cmp_ge_i32_e32 vcc, v214, v241
	v_cmp_lt_i32_e64 s[16:17], v214, v242
	s_and_b64 vcc, vcc, s[16:17]
	v_fmac_f32_e32 v78, 0x3e0293ee, v94
	v_cndmask_b32_e32 v78, v222, v78, vcc
	v_cmp_ge_i32_e32 vcc, v215, v241
	v_cmp_lt_i32_e64 s[16:17], v215, v242
	s_and_b64 vcc, vcc, s[16:17]
	v_fmac_f32_e32 v79, 0x3e0293ee, v95
	v_cndmask_b32_e32 v79, v222, v79, vcc
	v_cmp_ge_i32_e32 vcc, v216, v241
	v_cmp_lt_i32_e64 s[16:17], v216, v242
	s_and_b64 vcc, vcc, s[16:17]
	v_fmac_f32_e32 v80, 0x3e0293ee, v96
	v_cndmask_b32_e32 v80, v222, v80, vcc
	v_cmp_ge_i32_e32 vcc, v217, v241
	v_cmp_lt_i32_e64 s[16:17], v217, v242
	s_and_b64 vcc, vcc, s[16:17]
	v_fmac_f32_e32 v81, 0x3e0293ee, v97
	v_cndmask_b32_e32 v81, v222, v81, vcc
	v_max_f32_e32 v82, v78, v79
	v_max3_f32 v82, v82, v80, v81
	v_mov_b32_e32 v83, v82
	s_nop 1
	v_permlane32_swap_b32_e32 v82, v83
	v_max_f32_e32 v82, v82, v83
	v_sub_f32_e32 v83, v82, v244
	v_cmp_ge_f32_e32 vcc, s63, v83
	s_cmp_eq_u64 vcc, exec
	v_max_f32_e32 v82, v244, v82
	s_cselect_b64 vcc, -1, 0
	v_sub_f32_e32 v83, v244, v82
	v_cndmask_b32_e32 v244, v82, v244, vcc
	v_exp_f32_e32 v83, v83
	v_sub_f32_e32 v78, v78, v244
	v_exp_f32_e32 v78, v78
	v_sub_f32_e32 v79, v79, v244
	v_exp_f32_e32 v79, v79
	v_sub_f32_e32 v80, v80, v244
	v_exp_f32_e32 v80, v80
	v_sub_f32_e32 v81, v81, v244
	v_exp_f32_e32 v81, v81
	v_add_f32_e32 v82, v78, v79
	v_add_f32_e32 v82, v80, v82
	v_add_f32_e32 v242, v81, v82
	v_cndmask_b32_e64 v241, v83, 1.0, vcc
	v_mov_b32_e32 v243, v242
	v_mov_b32_e32 v66, 0
	v_mov_b32_e32 v67, 0
	v_mov_b32_e32 v68, 0
	v_mov_b32_e32 v69, 0
	v_mov_b32_e32 v70, 0
	v_mov_b32_e32 v71, 0
	v_cvt_pk_bf16_f32 v72, v78, v79
	v_cvt_pk_bf16_f32 v73, v80, v81
	s_branch .Lna_join_0

.LBB0_759:
	s_andn2_b64 vcc, exec, s[16:17]
	s_cbranch_vccnz .LBB0_793
	v_mov_b32_e32 v241, v190
	v_mov_b32_e32 v67, 0xff800000
	v_add_u32_e32 v242, 16, v241
	v_mov_b32_e32 v222, 0xff800000
	s_bitcmp1_b32 s82, 0
	s_cbranch_scc1 .Lna_minor_0
	ds_read_b32 v66, v237
	ds_read_b32 v67, v237 offset:4
	ds_read_b32 v68, v237 offset:8
	ds_read_b32 v69, v237 offset:12
	ds_read_b32 v70, v237 offset:32
	ds_read_b32 v71, v237 offset:36
	ds_read_b32 v72, v237 offset:40
	ds_read_b32 v73, v237 offset:44
	ds_read_b32 v74, v237 offset:64
	ds_read_b32 v75, v237 offset:68
	ds_read_b32 v76, v237 offset:72
	ds_read_b32 v77, v237 offset:76
	ds_read_b32 v78, v237 offset:96
	ds_read_b32 v79, v237 offset:100
	ds_read_b32 v80, v237 offset:104
	ds_read_b32 v81, v237 offset:108
	s_waitcnt lgkmcnt(0)
	v_cmp_ge_i32_e32 vcc, v181, v241
	v_cmp_lt_i32_e64 s[16:17], v181, v242
	s_and_b64 vcc, vcc, s[16:17]
	v_fmac_f32_e32 v66, 0x3e0293ee, v82
	v_cndmask_b32_e32 v66, v222, v66, vcc
	v_cmp_ge_i32_e32 vcc, v203, v241
	v_cmp_lt_i32_e64 s[16:17], v203, v242
	s_and_b64 vcc, vcc, s[16:17]
	v_fmac_f32_e32 v67, 0x3e0293ee, v83
	v_cndmask_b32_e32 v67, v222, v67, vcc
	v_cmp_ge_i32_e32 vcc, v204, v241
	v_cmp_lt_i32_e64 s[16:17], v204, v242
	s_and_b64 vcc, vcc, s[16:17]
	v_fmac_f32_e32 v68, 0x3e0293ee, v84
	v_cndmask_b32_e32 v68, v222, v68, vcc
	v_cmp_ge_i32_e32 vcc, v205, v241
	v_cmp_lt_i32_e64 s[16:17], v205, v242
	s_and_b64 vcc, vcc, s[16:17]
	v_fmac_f32_e32 v69, 0x3e0293ee, v85
	v_cndmask_b32_e32 v69, v222, v69, vcc
	v_cmp_ge_i32_e32 vcc, v206, v241
	v_cmp_lt_i32_e64 s[16:17], v206, v242
	s_and_b64 vcc, vcc, s[16:17]
	v_fmac_f32_e32 v70, 0x3e0293ee, v86
	v_cndmask_b32_e32 v70, v222, v70, vcc
	v_cmp_ge_i32_e32 vcc, v207, v241
	v_cmp_lt_i32_e64 s[16:17], v207, v242
	s_and_b64 vcc, vcc, s[16:17]
	v_fmac_f32_e32 v71, 0x3e0293ee, v87
	v_cndmask_b32_e32 v71, v222, v71, vcc
	v_cmp_ge_i32_e32 vcc, v208, v241
	v_cmp_lt_i32_e64 s[16:17], v208, v242
	s_and_b64 vcc, vcc, s[16:17]
	v_fmac_f32_e32 v72, 0x3e0293ee, v88
	v_cndmask_b32_e32 v72, v222, v72, vcc
	v_cmp_ge_i32_e32 vcc, v209, v241
	v_cmp_lt_i32_e64 s[16:17], v209, v242
	s_and_b64 vcc, vcc, s[16:17]
	v_fmac_f32_e32 v73, 0x3e0293ee, v89
	v_cndmask_b32_e32 v73, v222, v73, vcc
	v_cmp_ge_i32_e32 vcc, v210, v241
	v_cmp_lt_i32_e64 s[16:17], v181, v241
	s_and_b64 vcc, vcc, s[16:17]
	v_fmac_f32_e32 v74, 0x3e0293ee, v90
	v_cndmask_b32_e32 v74, v222, v74, vcc
	v_cmp_ge_i32_e32 vcc, v211, v241
	v_cmp_lt_i32_e64 s[16:17], v211, v242
	s_and_b64 vcc, vcc, s[16:17]
	v_fmac_f32_e32 v75, 0x3e0293ee, v91
	v_cndmask_b32_e32 v75, v222, v75, vcc
	v_cmp_ge_i32_e32 vcc, v212, v241
	v_cmp_lt_i32_e64 s[16:17], v212, v242
	s_and_b64 vcc, vcc, s[16:17]
	v_fmac_f32_e32 v76, 0x3e0293ee, v92
	v_cndmask_b32_e32 v76, v222, v76, vcc
	v_cmp_ge_i32_e32 vcc, v213, v241
	v_cmp_lt_i32_e64 s[16:17], v213, v242
	s_and_b64 vcc, vcc, s[16:17]
	v_fmac_f32_e32 v77, 0x3e0293ee, v93
	v_cndmask_b32_e32 v77, v222, v77, vcc
	v_cmp_ge_i32_e32 vcc, v214, v241
	v_cmp_lt_i32_e64 s[16:17], v214, v242
	s_and_b64 vcc, vcc, s[16:17]
	v_fmac_f32_e32 v78, 0x3e0293ee, v94
	v_cndmask_b32_e32 v78, v222, v78, vcc
	v_cmp_ge_i32_e32 vcc, v215, v241
	v_cmp_lt_i32_e64 s[16:17], v215, v242
	s_and_b64 vcc, vcc, s[16:17]
	v_fmac_f32_e32 v79, 0x3e0293ee, v95
	v_cndmask_b32_e32 v79, v222, v79, vcc
	v_cmp_ge_i32_e32 vcc, v216, v241
	v_cmp_lt_i32_e64 s[16:17], v216, v242
	s_and_b64 vcc, vcc, s[16:17]
	v_fmac_f32_e32 v80, 0x3e0293ee, v96
	v_cndmask_b32_e32 v80, v222, v80, vcc
	v_cmp_ge_i32_e32 vcc, v217, v241
	v_cmp_lt_i32_e64 s[16:17], v217, v242
	s_and_b64 vcc, vcc, s[16:17]
	v_fmac_f32_e32 v81, 0x3e0293ee, v97
	v_cndmask_b32_e32 v81, v222, v81, vcc

.Lna_join_0:
	s_nop 1
	v_permlane32_swap_b32_e32 v242, v243
	v_permlane32_swap_b32_e32 v66, v68
	v_permlane32_swap_b32_e32 v67, v69
	v_permlane32_swap_b32_e32 v70, v72
	v_permlane32_swap_b32_e32 v71, v73
	v_cmp_gt_f32_e32 vcc, 1.0, v241
	s_cbranch_vccz .LBB0_797
	s_and_saveexec_b64 s[16:17], s[10:11]
	ds_write_b32 v192, v241 offset:128
	s_or_b64 exec, exec, s[16:17]
	s_waitcnt lgkmcnt(0)
	ds_read_b128 v[74:77], v218 offset:224
	ds_read_b128 v[78:81], v218 offset:192
	ds_read_b128 v[82:85], v218 offset:160
	ds_read_b128 v[86:89], v218 offset:128
	s_waitcnt lgkmcnt(3)
	v_pk_mul_f32 v[62:63], v[62:63], v[76:77]
	s_waitcnt lgkmcnt(2)
	v_pk_mul_f32 v[58:59], v[58:59], v[80:81]
	s_waitcnt lgkmcnt(1)
	v_pk_mul_f32 v[54:55], v[54:55], v[84:85]
	s_waitcnt lgkmcnt(0)
	v_pk_mul_f32 v[50:51], v[50:51], v[88:89]
	v_pk_mul_f32 v[60:61], v[60:61], v[74:75]
	v_pk_mul_f32 v[56:57], v[56:57], v[78:79]
	v_pk_mul_f32 v[52:53], v[52:53], v[82:83]
	v_pk_mul_f32 v[48:49], v[48:49], v[86:87]
	v_pk_mul_f32 v[46:47], v[46:47], v[76:77]
	v_pk_mul_f32 v[42:43], v[42:43], v[80:81]
	v_pk_mul_f32 v[38:39], v[38:39], v[84:85]
	v_pk_mul_f32 v[34:35], v[34:35], v[88:89]
	v_pk_mul_f32 v[44:45], v[44:45], v[74:75]
	v_pk_mul_f32 v[40:41], v[40:41], v[78:79]
	v_pk_mul_f32 v[36:37], v[36:37], v[82:83]
	v_pk_mul_f32 v[32:33], v[32:33], v[86:87]
	v_pk_mul_f32 v[30:31], v[30:31], v[76:77]
	v_pk_mul_f32 v[26:27], v[26:27], v[80:81]
	v_pk_mul_f32 v[22:23], v[22:23], v[84:85]
	v_pk_mul_f32 v[18:19], v[18:19], v[88:89]
	v_pk_mul_f32 v[28:29], v[28:29], v[74:75]
	v_pk_mul_f32 v[24:25], v[24:25], v[78:79]
	v_pk_mul_f32 v[20:21], v[20:21], v[82:83]
	v_pk_mul_f32 v[16:17], v[16:17], v[86:87]
	v_pk_mul_f32 v[14:15], v[14:15], v[76:77]
	v_pk_mul_f32 v[10:11], v[10:11], v[80:81]
	v_pk_mul_f32 v[6:7], v[6:7], v[84:85]
	v_pk_mul_f32 v[2:3], v[2:3], v[88:89]
	v_pk_mul_f32 v[12:13], v[12:13], v[74:75]
	v_pk_mul_f32 v[8:9], v[8:9], v[78:79]
	v_pk_mul_f32 v[4:5], v[4:5], v[82:83]
	v_pk_mul_f32 v[0:1], v[0:1], v[86:87]

.LBB0_799:
	s_andn2_b64 vcc, exec, s[16:17]
	s_cbranch_vccnz .LBB0_833
	v_mov_b32_e32 v245, v190
	v_mov_b32_e32 v67, 0xff800000
	v_add_u32_e32 v246, 16, v245
	v_mov_b32_e32 v222, 0xff800000
	s_bitcmp1_b32 s82, 0
	s_cbranch_scc0 .Lna_minor_1
	ds_read_b32 v66, v237 offset:128
	ds_read_b32 v67, v237 offset:132
	ds_read_b32 v68, v237 offset:136
	ds_read_b32 v69, v237 offset:140
	ds_read_b32 v70, v237 offset:160
	ds_read_b32 v71, v237 offset:164
	ds_read_b32 v72, v237 offset:168
	ds_read_b32 v73, v237 offset:172
	ds_read_b32 v74, v237 offset:192
	ds_read_b32 v75, v237 offset:196
	ds_read_b32 v76, v237 offset:200
	ds_read_b32 v77, v237 offset:204
	ds_read_b32 v78, v237 offset:224
	ds_read_b32 v79, v237 offset:228
	ds_read_b32 v80, v237 offset:232
	ds_read_b32 v81, v237 offset:236
	s_waitcnt lgkmcnt(0)
	v_cmp_ge_i32_e32 vcc, v219, v245
	v_cmp_lt_i32_e64 s[12:13], v219, v246
	s_and_b64 vcc, vcc, s[12:13]
	v_fmac_f32_e32 v66, 0x3e0293ee, v82
	v_cndmask_b32_e32 v66, v222, v66, vcc
	v_cmp_ge_i32_e32 vcc, v220, v245
	v_cmp_lt_i32_e64 s[12:13], v220, v246
	s_and_b64 vcc, vcc, s[12:13]
	v_fmac_f32_e32 v67, 0x3e0293ee, v83
	v_cndmask_b32_e32 v67, v222, v67, vcc
	v_cmp_ge_i32_e32 vcc, v221, v245
	v_cmp_lt_i32_e64 s[12:13], v221, v246
	s_and_b64 vcc, vcc, s[12:13]
	v_fmac_f32_e32 v68, 0x3e0293ee, v84
	v_cndmask_b32_e32 v68, v222, v68, vcc
	v_cmp_ge_i32_e32 vcc, v223, v245
	v_cmp_lt_i32_e64 s[12:13], v223, v246
	s_and_b64 vcc, vcc, s[12:13]
	v_fmac_f32_e32 v69, 0x3e0293ee, v85
	v_cndmask_b32_e32 v69, v222, v69, vcc
	v_cmp_ge_i32_e32 vcc, v224, v245
	v_cmp_lt_i32_e64 s[12:13], v224, v246
	s_and_b64 vcc, vcc, s[12:13]
	v_fmac_f32_e32 v70, 0x3e0293ee, v86
	v_cndmask_b32_e32 v70, v222, v70, vcc
	v_cmp_ge_i32_e32 vcc, v225, v245
	v_cmp_lt_i32_e64 s[12:13], v225, v246
	s_and_b64 vcc, vcc, s[12:13]
	v_fmac_f32_e32 v71, 0x3e0293ee, v87
	v_cndmask_b32_e32 v71, v222, v71, vcc
	v_cmp_ge_i32_e32 vcc, v226, v245
	v_cmp_lt_i32_e64 s[12:13], v226, v246
	s_and_b64 vcc, vcc, s[12:13]
	v_fmac_f32_e32 v72, 0x3e0293ee, v88
	v_cndmask_b32_e32 v72, v222, v72, vcc
	v_cmp_ge_i32_e32 vcc, v227, v245
	v_cmp_lt_i32_e64 s[12:13], v227, v246
	s_and_b64 vcc, vcc, s[12:13]
	v_fmac_f32_e32 v73, 0x3e0293ee, v89
	v_cndmask_b32_e32 v73, v222, v73, vcc
	v_cmp_ge_i32_e32 vcc, v228, v245
	v_cmp_lt_i32_e64 s[12:13], v228, v246
	s_and_b64 vcc, vcc, s[12:13]
	v_fmac_f32_e32 v74, 0x3e0293ee, v90
	v_cndmask_b32_e32 v74, v222, v74, vcc
	v_cmp_ge_i32_e32 vcc, v229, v245
	v_cmp_lt_i32_e64 s[12:13], v229, v246
	s_and_b64 vcc, vcc, s[12:13]
	v_fmac_f32_e32 v75, 0x3e0293ee, v91
	v_cndmask_b32_e32 v75, v222, v75, vcc
	v_cmp_ge_i32_e32 vcc, v230, v245
	v_cmp_lt_i32_e64 s[12:13], v230, v246
	s_and_b64 vcc, vcc, s[12:13]
	v_fmac_f32_e32 v76, 0x3e0293ee, v92
	v_cndmask_b32_e32 v76, v222, v76, vcc
	v_cmp_ge_i32_e32 vcc, v231, v245
	v_cmp_lt_i32_e64 s[12:13], v231, v246
	s_and_b64 vcc, vcc, s[12:13]
	v_fmac_f32_e32 v77, 0x3e0293ee, v93
	v_cndmask_b32_e32 v77, v222, v77, vcc
	v_cmp_ge_i32_e32 vcc, v232, v245
	v_cmp_lt_i32_e64 s[12:13], v232, v246
	s_and_b64 vcc, vcc, s[12:13]
	v_fmac_f32_e32 v78, 0x3e0293ee, v94
	v_cndmask_b32_e32 v78, v222, v78, vcc
	v_cmp_ge_i32_e32 vcc, v233, v245
	v_cmp_lt_i32_e64 s[12:13], v233, v246
	s_and_b64 vcc, vcc, s[12:13]
	v_fmac_f32_e32 v79, 0x3e0293ee, v95
	v_cndmask_b32_e32 v79, v222, v79, vcc
	v_cmp_ge_i32_e32 vcc, v234, v245
	v_cmp_lt_i32_e64 s[12:13], v234, v246
	s_and_b64 vcc, vcc, s[12:13]
	v_fmac_f32_e32 v80, 0x3e0293ee, v96
	v_cndmask_b32_e32 v80, v222, v80, vcc
	v_cmp_ge_i32_e32 vcc, v235, v245
	v_cmp_lt_i32_e64 s[12:13], v235, v246
	s_and_b64 vcc, vcc, s[12:13]
	v_fmac_f32_e32 v81, 0x3e0293ee, v97
	v_cndmask_b32_e32 v81, v222, v81, vcc

.Lna_join_1:
	s_nop 1
	v_permlane32_swap_b32_e32 v75, v76
	v_permlane32_swap_b32_e32 v66, v68
	v_permlane32_swap_b32_e32 v67, v69
	v_permlane32_swap_b32_e32 v70, v72
	v_permlane32_swap_b32_e32 v71, v73
	v_cmp_gt_f32_e32 vcc, 1.0, v74
	s_cbranch_vccz .LBB0_837
	s_and_saveexec_b64 s[12:13], s[10:11]
	ds_write_b32 v192, v74 offset:128
	s_or_b64 exec, exec, s[12:13]
	s_waitcnt lgkmcnt(0)
	ds_read_b128 v[78:81], v218 offset:224
	ds_read_b128 v[82:85], v218 offset:192
	ds_read_b128 v[86:89], v218 offset:160
	ds_read_b128 v[90:93], v218 offset:128
	s_waitcnt lgkmcnt(3)
	v_pk_mul_f32 v[62:63], v[62:63], v[80:81]
	s_waitcnt lgkmcnt(2)
	v_pk_mul_f32 v[58:59], v[58:59], v[84:85]
	s_waitcnt lgkmcnt(1)
	v_pk_mul_f32 v[54:55], v[54:55], v[88:89]
	s_waitcnt lgkmcnt(0)
	v_pk_mul_f32 v[50:51], v[50:51], v[92:93]
	v_pk_mul_f32 v[60:61], v[60:61], v[78:79]
	v_pk_mul_f32 v[56:57], v[56:57], v[82:83]
	v_pk_mul_f32 v[52:53], v[52:53], v[86:87]
	v_pk_mul_f32 v[48:49], v[48:49], v[90:91]
	v_pk_mul_f32 v[46:47], v[46:47], v[80:81]
	v_pk_mul_f32 v[42:43], v[42:43], v[84:85]
	v_pk_mul_f32 v[38:39], v[38:39], v[88:89]
	v_pk_mul_f32 v[34:35], v[34:35], v[92:93]
	v_pk_mul_f32 v[44:45], v[44:45], v[78:79]
	v_pk_mul_f32 v[40:41], v[40:41], v[82:83]
	v_pk_mul_f32 v[36:37], v[36:37], v[86:87]
	v_pk_mul_f32 v[32:33], v[32:33], v[90:91]
	v_pk_mul_f32 v[30:31], v[30:31], v[80:81]
	v_pk_mul_f32 v[26:27], v[26:27], v[84:85]
	v_pk_mul_f32 v[22:23], v[22:23], v[88:89]
	v_pk_mul_f32 v[18:19], v[18:19], v[92:93]
	v_pk_mul_f32 v[28:29], v[28:29], v[78:79]
	v_pk_mul_f32 v[24:25], v[24:25], v[82:83]
	v_pk_mul_f32 v[20:21], v[20:21], v[86:87]
	v_pk_mul_f32 v[16:17], v[16:17], v[90:91]
	v_pk_mul_f32 v[14:15], v[14:15], v[80:81]
	v_pk_mul_f32 v[10:11], v[10:11], v[84:85]
	v_pk_mul_f32 v[6:7], v[6:7], v[88:89]
	v_pk_mul_f32 v[2:3], v[2:3], v[92:93]
	v_pk_mul_f32 v[12:13], v[12:13], v[78:79]
	v_pk_mul_f32 v[8:9], v[8:9], v[82:83]
	v_pk_mul_f32 v[4:5], v[4:5], v[86:87]
	v_pk_mul_f32 v[0:1], v[0:1], v[90:91]

.Lna_minor_3:
	ds_read_b32 v82, v240 offset:128
	ds_read_b32 v83, v240 offset:132
	ds_read_b32 v84, v240 offset:136
	ds_read_b32 v85, v240 offset:140
	s_waitcnt lgkmcnt(0)
	v_cmp_ge_i32_e32 vcc, v223, v245
	v_cmp_lt_i32_e64 s[12:13], v223, v246
	s_and_b64 vcc, vcc, s[12:13]
	v_fmac_f32_e32 v82, 0x3e0293ee, v98
	v_cndmask_b32_e32 v82, v222, v82, vcc
	v_cmp_ge_i32_e32 vcc, v224, v245
	v_cmp_lt_i32_e64 s[12:13], v224, v246
	s_and_b64 vcc, vcc, s[12:13]
	v_fmac_f32_e32 v83, 0x3e0293ee, v99
	v_cndmask_b32_e32 v83, v222, v83, vcc
	v_cmp_ge_i32_e32 vcc, v225, v245
	v_cmp_lt_i32_e64 s[12:13], v225, v246
	s_and_b64 vcc, vcc, s[12:13]
	v_fmac_f32_e32 v84, 0x3e0293ee, v100
	v_cndmask_b32_e32 v84, v222, v84, vcc
	v_cmp_ge_i32_e32 vcc, v226, v245
	v_cmp_lt_i32_e64 s[12:13], v226, v246
	s_and_b64 vcc, vcc, s[12:13]
	v_fmac_f32_e32 v85, 0x3e0293ee, v101
	v_cndmask_b32_e32 v85, v222, v85, vcc
	v_max_f32_e32 v98, v82, v83
	v_max3_f32 v98, v98, v84, v85
	v_mov_b32_e32 v99, v98
	s_nop 1
	v_permlane32_swap_b32_e32 v98, v99
	v_max_f32_e32 v98, v98, v99
	v_sub_f32_e32 v99, v98, v244
	v_cmp_ge_f32_e32 vcc, s61, v99
	s_cmp_eq_u64 vcc, exec
	v_max_f32_e32 v98, v244, v98
	s_cselect_b64 vcc, -1, 0
	v_sub_f32_e32 v99, v244, v98
	v_cndmask_b32_e32 v244, v98, v244, vcc
	v_exp_f32_e32 v99, v99
	v_sub_f32_e32 v82, v82, v244
	v_exp_f32_e32 v82, v82
	v_sub_f32_e32 v83, v83, v244
	v_exp_f32_e32 v83, v83
	v_sub_f32_e32 v84, v84, v244
	v_exp_f32_e32 v84, v84
	v_sub_f32_e32 v85, v85, v244
	v_exp_f32_e32 v85, v85
	v_add_f32_e32 v98, v82, v83
	v_add_f32_e32 v98, v84, v98
	v_add_f32_e32 v91, v85, v98
	v_cndmask_b32_e64 v90, v99, 1.0, vcc
	v_mov_b32_e32 v92, v91
	v_cvt_pk_bf16_f32 v82, v82, v83
	v_cvt_pk_bf16_f32 v83, v84, v85
	v_mov_b32_e32 v84, 0
	v_mov_b32_e32 v85, 0
	v_mov_b32_e32 v86, 0
	v_mov_b32_e32 v87, 0
	v_mov_b32_e32 v88, 0
	v_mov_b32_e32 v89, 0
	s_branch .Lna_join_3
.Lna_minor_2:
	ds_read_b32 v94, v240 offset:96
	ds_read_b32 v95, v240 offset:100
	ds_read_b32 v96, v240 offset:104
	ds_read_b32 v97, v240 offset:108
	s_waitcnt lgkmcnt(0)
	v_cmp_ge_i32_e32 vcc, v217, v14
	v_cmp_lt_i32_e64 s[16:17], v217, v15
	s_and_b64 vcc, vcc, s[16:17]
	v_fmac_f32_e32 v94, 0x3e0293ee, v110
	v_cndmask_b32_e32 v94, v222, v94, vcc
	v_cmp_ge_i32_e32 vcc, v218, v14
	v_cmp_lt_i32_e64 s[16:17], v218, v15
	s_and_b64 vcc, vcc, s[16:17]
	v_fmac_f32_e32 v95, 0x3e0293ee, v111
	v_cndmask_b32_e32 v95, v222, v95, vcc
	v_cmp_ge_i32_e32 vcc, v219, v14
	v_cmp_lt_i32_e64 s[16:17], v219, v15
	s_and_b64 vcc, vcc, s[16:17]
	v_fmac_f32_e32 v96, 0x3e0293ee, v112
	v_cndmask_b32_e32 v96, v222, v96, vcc
	v_cmp_ge_i32_e32 vcc, v220, v14
	v_cmp_lt_i32_e64 s[16:17], v220, v15
	s_and_b64 vcc, vcc, s[16:17]
	v_fmac_f32_e32 v97, 0x3e0293ee, v113
	v_cndmask_b32_e32 v97, v222, v97, vcc
	v_max_f32_e32 v14, v94, v95
	v_max3_f32 v14, v14, v96, v97
	v_mov_b32_e32 v15, v14
	s_nop 1
	v_permlane32_swap_b32_e32 v14, v15
	v_max_f32_e32 v14, v14, v15
	v_sub_f32_e32 v15, v14, v244
	v_cmp_ge_f32_e32 vcc, s61, v15
	s_cmp_eq_u64 vcc, exec
	v_max_f32_e32 v14, v244, v14
	s_cselect_b64 vcc, -1, 0
	v_sub_f32_e32 v15, v244, v14
	v_cndmask_b32_e32 v244, v14, v244, vcc
	v_exp_f32_e32 v98, v15
	v_sub_f32_e32 v94, v94, v244
	v_exp_f32_e32 v94, v94
	v_sub_f32_e32 v95, v95, v244
	v_exp_f32_e32 v95, v95
	v_sub_f32_e32 v96, v96, v244
	v_exp_f32_e32 v96, v96
	v_sub_f32_e32 v97, v97, v244
	v_exp_f32_e32 v97, v97
	v_add_f32_e32 v14, v94, v95
	v_add_f32_e32 v14, v96, v14
	v_add_f32_e32 v15, v97, v14
	v_cndmask_b32_e64 v14, v98, 1.0, vcc
	v_mov_b32_e32 v243, v15
	v_mov_b32_e32 v82, 0
	v_mov_b32_e32 v83, 0
	v_mov_b32_e32 v84, 0
	v_mov_b32_e32 v85, 0
	v_mov_b32_e32 v86, 0
	v_mov_b32_e32 v87, 0
	v_cvt_pk_bf16_f32 v88, v94, v95
	v_cvt_pk_bf16_f32 v89, v96, v97
	s_branch .Lna_join_2

.LBB0_2043:
	s_andn2_b64 vcc, exec, s[16:17]
	s_cbranch_vccnz .LBB0_2077
	v_mov_b32_e32 v14, v192
	v_mov_b32_e32 v83, 0xff800000
	v_add_u32_e32 v15, 16, v14
	v_mov_b32_e32 v222, 0xff800000
	s_bitcmp1_b32 s82, 0
	s_cbranch_scc1 .Lna_minor_2
	ds_read_b32 v82, v240
	ds_read_b32 v83, v240 offset:4
	ds_read_b32 v84, v240 offset:8
	ds_read_b32 v85, v240 offset:12
	ds_read_b32 v86, v240 offset:32
	ds_read_b32 v87, v240 offset:36
	ds_read_b32 v88, v240 offset:40
	ds_read_b32 v89, v240 offset:44
	ds_read_b32 v90, v240 offset:64
	ds_read_b32 v91, v240 offset:68
	ds_read_b32 v92, v240 offset:72
	ds_read_b32 v93, v240 offset:76
	ds_read_b32 v94, v240 offset:96
	ds_read_b32 v95, v240 offset:100
	ds_read_b32 v96, v240 offset:104
	ds_read_b32 v97, v240 offset:108
	s_waitcnt lgkmcnt(0)
	v_cmp_ge_i32_e32 vcc, v194, v14
	v_cmp_lt_i32_e64 s[16:17], v194, v15
	s_and_b64 vcc, vcc, s[16:17]
	v_fmac_f32_e32 v82, 0x3e0293ee, v98
	v_cndmask_b32_e32 v82, v222, v82, vcc
	v_cmp_ge_i32_e32 vcc, v206, v14
	v_cmp_lt_i32_e64 s[16:17], v206, v15
	s_and_b64 vcc, vcc, s[16:17]
	v_fmac_f32_e32 v83, 0x3e0293ee, v99
	v_cndmask_b32_e32 v83, v222, v83, vcc
	v_cmp_ge_i32_e32 vcc, v207, v14
	v_cmp_lt_i32_e64 s[16:17], v207, v15
	s_and_b64 vcc, vcc, s[16:17]
	v_fmac_f32_e32 v84, 0x3e0293ee, v100
	v_cndmask_b32_e32 v84, v222, v84, vcc
	v_cmp_ge_i32_e32 vcc, v208, v14
	v_cmp_lt_i32_e64 s[16:17], v208, v15
	s_and_b64 vcc, vcc, s[16:17]
	v_fmac_f32_e32 v85, 0x3e0293ee, v101
	v_cndmask_b32_e32 v85, v222, v85, vcc
	v_cmp_ge_i32_e32 vcc, v209, v14
	v_cmp_lt_i32_e64 s[16:17], v209, v15
	s_and_b64 vcc, vcc, s[16:17]
	v_fmac_f32_e32 v86, 0x3e0293ee, v102
	v_cndmask_b32_e32 v86, v222, v86, vcc
	v_cmp_ge_i32_e32 vcc, v210, v14
	v_cmp_lt_i32_e64 s[16:17], v210, v15
	s_and_b64 vcc, vcc, s[16:17]
	v_fmac_f32_e32 v87, 0x3e0293ee, v103
	v_cndmask_b32_e32 v87, v222, v87, vcc
	v_cmp_ge_i32_e32 vcc, v211, v14
	v_cmp_lt_i32_e64 s[16:17], v211, v15
	s_and_b64 vcc, vcc, s[16:17]
	v_fmac_f32_e32 v88, 0x3e0293ee, v104
	v_cndmask_b32_e32 v88, v222, v88, vcc
	v_cmp_ge_i32_e32 vcc, v212, v14
	v_cmp_lt_i32_e64 s[16:17], v212, v15
	s_and_b64 vcc, vcc, s[16:17]
	v_fmac_f32_e32 v89, 0x3e0293ee, v105
	v_cndmask_b32_e32 v89, v222, v89, vcc
	v_cmp_ge_i32_e32 vcc, v213, v14
	v_cmp_lt_i32_e64 s[16:17], v194, v14
	s_and_b64 vcc, vcc, s[16:17]
	v_fmac_f32_e32 v90, 0x3e0293ee, v106
	v_cndmask_b32_e32 v90, v222, v90, vcc
	v_cmp_ge_i32_e32 vcc, v214, v14
	v_cmp_lt_i32_e64 s[16:17], v214, v15
	s_and_b64 vcc, vcc, s[16:17]
	v_fmac_f32_e32 v91, 0x3e0293ee, v107
	v_cndmask_b32_e32 v91, v222, v91, vcc
	v_cmp_ge_i32_e32 vcc, v215, v14
	v_cmp_lt_i32_e64 s[16:17], v215, v15
	s_and_b64 vcc, vcc, s[16:17]
	v_fmac_f32_e32 v92, 0x3e0293ee, v108
	v_cndmask_b32_e32 v92, v222, v92, vcc
	v_cmp_ge_i32_e32 vcc, v216, v14
	v_cmp_lt_i32_e64 s[16:17], v216, v15
	s_and_b64 vcc, vcc, s[16:17]
	v_fmac_f32_e32 v93, 0x3e0293ee, v109
	v_cndmask_b32_e32 v93, v222, v93, vcc
	v_cmp_ge_i32_e32 vcc, v217, v14
	v_cmp_lt_i32_e64 s[16:17], v217, v15
	s_and_b64 vcc, vcc, s[16:17]
	v_fmac_f32_e32 v94, 0x3e0293ee, v110
	v_cndmask_b32_e32 v94, v222, v94, vcc
	v_cmp_ge_i32_e32 vcc, v218, v14
	v_cmp_lt_i32_e64 s[16:17], v218, v15
	s_and_b64 vcc, vcc, s[16:17]
	v_fmac_f32_e32 v95, 0x3e0293ee, v111
	v_cndmask_b32_e32 v95, v222, v95, vcc
	v_cmp_ge_i32_e32 vcc, v219, v14
	v_cmp_lt_i32_e64 s[16:17], v219, v15
	s_and_b64 vcc, vcc, s[16:17]
	v_fmac_f32_e32 v96, 0x3e0293ee, v112
	v_cndmask_b32_e32 v96, v222, v96, vcc
	v_cmp_ge_i32_e32 vcc, v220, v14
	v_cmp_lt_i32_e64 s[16:17], v220, v15
	s_and_b64 vcc, vcc, s[16:17]
	v_fmac_f32_e32 v97, 0x3e0293ee, v113
	v_cndmask_b32_e32 v97, v222, v97, vcc

.Lna_join_2:
	s_nop 1
	v_permlane32_swap_b32_e32 v15, v243
	v_permlane32_swap_b32_e32 v82, v84
	v_permlane32_swap_b32_e32 v83, v85
	v_permlane32_swap_b32_e32 v86, v88
	v_permlane32_swap_b32_e32 v87, v89
	v_cmp_gt_f32_e32 vcc, 1.0, v14
	s_cbranch_vccz .LBB0_2081
	s_and_saveexec_b64 s[16:17], s[10:11]
	ds_write_b32 v196, v14 offset:128
	s_or_b64 exec, exec, s[16:17]
	s_waitcnt lgkmcnt(0)
	ds_read_b128 v[90:93], v221 offset:224
	ds_read_b128 v[94:97], v221 offset:192
	ds_read_b128 v[98:101], v221 offset:160
	ds_read_b128 v[102:105], v221 offset:128
	s_waitcnt lgkmcnt(3)
	v_pk_mul_f32 v[78:79], v[78:79], v[92:93]
	s_waitcnt lgkmcnt(2)
	v_pk_mul_f32 v[74:75], v[74:75], v[96:97]
	s_waitcnt lgkmcnt(1)
	v_pk_mul_f32 v[70:71], v[70:71], v[100:101]
	s_waitcnt lgkmcnt(0)
	v_pk_mul_f32 v[66:67], v[66:67], v[104:105]
	v_pk_mul_f32 v[76:77], v[76:77], v[90:91]
	v_pk_mul_f32 v[72:73], v[72:73], v[94:95]
	v_pk_mul_f32 v[68:69], v[68:69], v[98:99]
	v_pk_mul_f32 v[64:65], v[64:65], v[102:103]
	v_pk_mul_f32 v[62:63], v[62:63], v[92:93]
	v_pk_mul_f32 v[58:59], v[58:59], v[96:97]
	v_pk_mul_f32 v[54:55], v[54:55], v[100:101]
	v_pk_mul_f32 v[50:51], v[50:51], v[104:105]
	v_pk_mul_f32 v[60:61], v[60:61], v[90:91]
	v_pk_mul_f32 v[56:57], v[56:57], v[94:95]
	v_pk_mul_f32 v[52:53], v[52:53], v[98:99]
	v_pk_mul_f32 v[48:49], v[48:49], v[102:103]
	v_pk_mul_f32 v[46:47], v[46:47], v[92:93]
	v_pk_mul_f32 v[42:43], v[42:43], v[96:97]
	v_pk_mul_f32 v[38:39], v[38:39], v[100:101]
	v_pk_mul_f32 v[34:35], v[34:35], v[104:105]
	v_pk_mul_f32 v[44:45], v[44:45], v[90:91]
	v_pk_mul_f32 v[40:41], v[40:41], v[94:95]
	v_pk_mul_f32 v[36:37], v[36:37], v[98:99]
	v_pk_mul_f32 v[32:33], v[32:33], v[102:103]
	v_pk_mul_f32 v[30:31], v[30:31], v[92:93]
	v_pk_mul_f32 v[26:27], v[26:27], v[96:97]
	v_pk_mul_f32 v[22:23], v[22:23], v[100:101]
	v_pk_mul_f32 v[18:19], v[18:19], v[104:105]
	v_pk_mul_f32 v[28:29], v[28:29], v[90:91]
	v_pk_mul_f32 v[24:25], v[24:25], v[94:95]
	v_pk_mul_f32 v[20:21], v[20:21], v[98:99]
	v_pk_mul_f32 v[16:17], v[16:17], v[102:103]

.LBB0_2083:
	s_andn2_b64 vcc, exec, s[16:17]
	s_cbranch_vccnz .LBB0_2117
	v_mov_b32_e32 v245, v192
	v_mov_b32_e32 v83, 0xff800000
	v_add_u32_e32 v246, 16, v245
	v_mov_b32_e32 v222, 0xff800000
	s_bitcmp1_b32 s82, 0
	s_cbranch_scc0 .Lna_minor_3
	ds_read_b32 v82, v240 offset:128
	ds_read_b32 v83, v240 offset:132
	ds_read_b32 v84, v240 offset:136
	ds_read_b32 v85, v240 offset:140
	ds_read_b32 v86, v240 offset:160
	ds_read_b32 v87, v240 offset:164
	ds_read_b32 v88, v240 offset:168
	ds_read_b32 v89, v240 offset:172
	ds_read_b32 v90, v240 offset:192
	ds_read_b32 v91, v240 offset:196
	ds_read_b32 v92, v240 offset:200
	ds_read_b32 v93, v240 offset:204
	ds_read_b32 v94, v240 offset:224
	ds_read_b32 v95, v240 offset:228
	ds_read_b32 v96, v240 offset:232
	ds_read_b32 v97, v240 offset:236
	s_waitcnt lgkmcnt(0)
	v_cmp_ge_i32_e32 vcc, v223, v245
	v_cmp_lt_i32_e64 s[12:13], v223, v246
	s_and_b64 vcc, vcc, s[12:13]
	v_fmac_f32_e32 v82, 0x3e0293ee, v98
	v_cndmask_b32_e32 v82, v222, v82, vcc
	v_cmp_ge_i32_e32 vcc, v224, v245
	v_cmp_lt_i32_e64 s[12:13], v224, v246
	s_and_b64 vcc, vcc, s[12:13]
	v_fmac_f32_e32 v83, 0x3e0293ee, v99
	v_cndmask_b32_e32 v83, v222, v83, vcc
	v_cmp_ge_i32_e32 vcc, v225, v245
	v_cmp_lt_i32_e64 s[12:13], v225, v246
	s_and_b64 vcc, vcc, s[12:13]
	v_fmac_f32_e32 v84, 0x3e0293ee, v100
	v_cndmask_b32_e32 v84, v222, v84, vcc
	v_cmp_ge_i32_e32 vcc, v226, v245
	v_cmp_lt_i32_e64 s[12:13], v226, v246
	s_and_b64 vcc, vcc, s[12:13]
	v_fmac_f32_e32 v85, 0x3e0293ee, v101
	v_cndmask_b32_e32 v85, v222, v85, vcc
	v_cmp_ge_i32_e32 vcc, v227, v245
	v_cmp_lt_i32_e64 s[12:13], v227, v246
	s_and_b64 vcc, vcc, s[12:13]
	v_fmac_f32_e32 v86, 0x3e0293ee, v102
	v_cndmask_b32_e32 v86, v222, v86, vcc
	v_cmp_ge_i32_e32 vcc, v228, v245
	v_cmp_lt_i32_e64 s[12:13], v228, v246
	s_and_b64 vcc, vcc, s[12:13]
	v_fmac_f32_e32 v87, 0x3e0293ee, v103
	v_cndmask_b32_e32 v87, v222, v87, vcc
	v_cmp_ge_i32_e32 vcc, v229, v245
	v_cmp_lt_i32_e64 s[12:13], v229, v246
	s_and_b64 vcc, vcc, s[12:13]
	v_fmac_f32_e32 v88, 0x3e0293ee, v104
	v_cndmask_b32_e32 v88, v222, v88, vcc
	v_cmp_ge_i32_e32 vcc, v230, v245
	v_cmp_lt_i32_e64 s[12:13], v230, v246
	s_and_b64 vcc, vcc, s[12:13]
	v_fmac_f32_e32 v89, 0x3e0293ee, v105
	v_cndmask_b32_e32 v89, v222, v89, vcc
	v_cmp_ge_i32_e32 vcc, v231, v245
	v_cmp_lt_i32_e64 s[12:13], v231, v246
	s_and_b64 vcc, vcc, s[12:13]
	v_fmac_f32_e32 v90, 0x3e0293ee, v106
	v_cndmask_b32_e32 v90, v222, v90, vcc
	v_cmp_ge_i32_e32 vcc, v232, v245
	v_cmp_lt_i32_e64 s[12:13], v232, v246
	s_and_b64 vcc, vcc, s[12:13]
	v_fmac_f32_e32 v91, 0x3e0293ee, v107
	v_cndmask_b32_e32 v91, v222, v91, vcc
	v_cmp_ge_i32_e32 vcc, v233, v245
	v_cmp_lt_i32_e64 s[12:13], v233, v246
	s_and_b64 vcc, vcc, s[12:13]
	v_fmac_f32_e32 v92, 0x3e0293ee, v108
	v_cndmask_b32_e32 v92, v222, v92, vcc
	v_cmp_ge_i32_e32 vcc, v234, v245
	v_cmp_lt_i32_e64 s[12:13], v234, v246
	s_and_b64 vcc, vcc, s[12:13]
	v_fmac_f32_e32 v93, 0x3e0293ee, v109
	v_cndmask_b32_e32 v93, v222, v93, vcc
	v_cmp_ge_i32_e32 vcc, v235, v245
	v_cmp_lt_i32_e64 s[12:13], v235, v246
	s_and_b64 vcc, vcc, s[12:13]
	v_fmac_f32_e32 v94, 0x3e0293ee, v110
	v_cndmask_b32_e32 v94, v222, v94, vcc
	v_cmp_ge_i32_e32 vcc, v236, v245
	v_cmp_lt_i32_e64 s[12:13], v236, v246
	s_and_b64 vcc, vcc, s[12:13]
	v_fmac_f32_e32 v95, 0x3e0293ee, v111
	v_cndmask_b32_e32 v95, v222, v95, vcc
	v_cmp_ge_i32_e32 vcc, v237, v245
	v_cmp_lt_i32_e64 s[12:13], v237, v246
	s_and_b64 vcc, vcc, s[12:13]
	v_fmac_f32_e32 v96, 0x3e0293ee, v112
	v_cndmask_b32_e32 v96, v222, v96, vcc
	v_cmp_ge_i32_e32 vcc, v238, v245
	v_cmp_lt_i32_e64 s[12:13], v238, v246
	s_and_b64 vcc, vcc, s[12:13]
	v_fmac_f32_e32 v97, 0x3e0293ee, v113
	v_cndmask_b32_e32 v97, v222, v97, vcc

.Lna_join_3:
	s_nop 1
	v_permlane32_swap_b32_e32 v91, v92
	v_permlane32_swap_b32_e32 v82, v84
	v_permlane32_swap_b32_e32 v83, v85
	v_permlane32_swap_b32_e32 v86, v88
	v_permlane32_swap_b32_e32 v87, v89
	v_cmp_gt_f32_e32 vcc, 1.0, v90
	s_cbranch_vccz .LBB0_2121
	s_and_saveexec_b64 s[12:13], s[10:11]
	ds_write_b32 v196, v90 offset:128
	s_or_b64 exec, exec, s[12:13]
	s_waitcnt lgkmcnt(0)
	ds_read_b128 v[94:97], v221 offset:224
	ds_read_b128 v[98:101], v221 offset:192
	ds_read_b128 v[102:105], v221 offset:160
	ds_read_b128 v[106:109], v221 offset:128
	s_waitcnt lgkmcnt(3)
	v_pk_mul_f32 v[78:79], v[78:79], v[96:97]
	s_waitcnt lgkmcnt(2)
	v_pk_mul_f32 v[74:75], v[74:75], v[100:101]
	s_waitcnt lgkmcnt(1)
	v_pk_mul_f32 v[70:71], v[70:71], v[104:105]
	s_waitcnt lgkmcnt(0)
	v_pk_mul_f32 v[66:67], v[66:67], v[108:109]
	v_pk_mul_f32 v[76:77], v[76:77], v[94:95]
	v_pk_mul_f32 v[72:73], v[72:73], v[98:99]
	v_pk_mul_f32 v[68:69], v[68:69], v[102:103]
	v_pk_mul_f32 v[64:65], v[64:65], v[106:107]
	v_pk_mul_f32 v[62:63], v[62:63], v[96:97]
	v_pk_mul_f32 v[58:59], v[58:59], v[100:101]
	v_pk_mul_f32 v[54:55], v[54:55], v[104:105]
	v_pk_mul_f32 v[50:51], v[50:51], v[108:109]
	v_pk_mul_f32 v[60:61], v[60:61], v[94:95]
	v_pk_mul_f32 v[56:57], v[56:57], v[98:99]
	v_pk_mul_f32 v[52:53], v[52:53], v[102:103]
	v_pk_mul_f32 v[48:49], v[48:49], v[106:107]
	v_pk_mul_f32 v[46:47], v[46:47], v[96:97]
	v_pk_mul_f32 v[42:43], v[42:43], v[100:101]
	v_pk_mul_f32 v[38:39], v[38:39], v[104:105]
	v_pk_mul_f32 v[34:35], v[34:35], v[108:109]
	v_pk_mul_f32 v[44:45], v[44:45], v[94:95]
	v_pk_mul_f32 v[40:41], v[40:41], v[98:99]
	v_pk_mul_f32 v[36:37], v[36:37], v[102:103]
	v_pk_mul_f32 v[32:33], v[32:33], v[106:107]
	v_pk_mul_f32 v[30:31], v[30:31], v[96:97]
	v_pk_mul_f32 v[26:27], v[26:27], v[100:101]
	v_pk_mul_f32 v[22:23], v[22:23], v[104:105]
	v_pk_mul_f32 v[18:19], v[18:19], v[108:109]
	v_pk_mul_f32 v[28:29], v[28:29], v[94:95]
	v_pk_mul_f32 v[24:25], v[24:25], v[98:99]
	v_pk_mul_f32 v[20:21], v[20:21], v[102:103]
	v_pk_mul_f32 v[16:17], v[16:17], v[106:107]
